# attention item loop: loop-top wait no longer covers the previous item's 8 output stores (vmcnt(8)), full drain moved to loop entry
# speedup vs baseline: 1.0060x; 1.0060x over previous
; #define LAS __attribute__((address_space(3)))
; __device__ __forceinline__ void ph_attn_mfma(const Frame& F) {
;     ...
;     const int tid = (F.wave * 64 + fresh_lane()), lane = tid & 63, wave = F.wave;
;     const int l15 = lane & 15, g = lane >> 4;
;     const float sc2 = 0.08838834764831845f * 1.4426950408889634f;
;     v4u kreg[8], va[4], vb[4], qn[4];
;     const int vb0 = (F.nwg % 8 == 0) ? ((F.bid % 8) * (F.nwg / 8) + F.bid / 8) : F.bid;
;     const int per = (3072 + F.nwg - 1) / F.nwg, ibase = vb0 * per, iend = (ibase + per < 3072) ? ibase + per : 3072;
;     int px = 0; AttnItem itp = attn_decode(0); bool havep = false;
;     if (ibase < iend) { const AttnItem it0 = attn_decode(ibase); attn_issue(HB, it0, tid, kreg, va, vb, false); attn_issue_q(HB, it0, tid, qn); }
;     for (int item = ibase; item < iend; ++item) {
;         const AttnItem it = attn_decode(item);
;         const bool cont = havep && attn_cont(it, itp);
;         px = cont ? (px ^ 1) : 0;
;         itp = it; havep = true;
;         const int hd = it.hd, br = it.br, dsh = it.dsh, blk = it.blk, tok0 = it.tok0;
;         const int qtok = tok0 + ((blk * 128 + wave * 16 + l15) << dsh);
;         v4u qf[4];
; #pragma unroll
;         for (int st = 0; st < 4; ++st) qf[st] = qn[st];
;         __syncthreads();
; #pragma unroll
;         for (int i = 0; i < 8; ++i) { if (cont && i < 4) continue; const int c = tid + 512 * i, kj = (c >> 4) ^ (px << 7), ch = c & 15; *(LAS v4u*)(lds + AT_K_OFF + kj * AT_KROW + ch * 16) = kreg[i]; }
; #pragma unroll
;         for (int i = 0; i < 4; ++i) {
;             if (cont && i < 2) continue;
;             const int u = tid + 512 * i;
;             const int kp = (((u >> 8) << 4) | (u & 15)) ^ (px << 6), ch = (((u >> 6) & 3) << 2) | ((u >> 4) & 3);
;             const v4u a = va[i], bb = vb[i];
;             LAS unsigned char* vbp = lds + AT_V_OFF + (ch * 8) * AT_VROW + kp * 4;
;             *(LAS unsigned*)(vbp + 0 * AT_VROW) = (a.x & 0xffffu) | (bb.x << 16);      *(LAS unsigned*)(vbp + 1 * AT_VROW) = (a.x >> 16) | (bb.x & 0xffff0000u);
;             *(LAS unsigned*)(vbp + 2 * AT_VROW) = (a.y & 0xffffu) | (bb.y << 16);      *(LAS unsigned*)(vbp + 3 * AT_VROW) = (a.y >> 16) | (bb.y & 0xffff0000u);
;             *(LAS unsigned*)(vbp + 4 * AT_VROW) = (a.z & 0xffffu) | (bb.z << 16);      *(LAS unsigned*)(vbp + 5 * AT_VROW) = (a.z >> 16) | (bb.z & 0xffff0000u);
.LBB0_859:
	v_lshlrev_b32_e32 v0, 4, v85
	v_writelane_b32 v254, s36, 63
	v_and_b32_e32 v0, 0xf0, v0
	v_bfe_u32 v2, v85, 4, 2
	v_add_u32_e32 v122, 0, v0
	v_lshrrev_b32_e32 v0, 4, v86
	v_readlane_b32 s6, v254, 50
	v_and_or_b32 v0, v0, 12, v2
	s_add_u32 s12, s60, 0x1c600000
	v_mov_b32_e32 v3, s6
	s_movk_i32 s6, 0x1080
	v_mad_u32_u24 v125, v0, s6, v3
	v_add_u32_e32 v0, 0x200, v86
	v_ashrrev_i32_e32 v132, 4, v0
	v_add_u32_e32 v0, 0x400, v86
	v_ashrrev_i32_e32 v134, 4, v0
	v_add_u32_e32 v0, 0x600, v86
	v_ashrrev_i32_e32 v136, 4, v0
	v_add_u32_e32 v0, 0x800, v86
	v_ashrrev_i32_e32 v138, 4, v0
	v_add_u32_e32 v0, 0xa00, v86
	v_ashrrev_i32_e32 v140, 4, v0
	v_add_u32_e32 v0, 0xc00, v86
	v_ashrrev_i32_e32 v142, 4, v0
	v_add_u32_e32 v0, 0xe00, v86
	v_writelane_b32 v255, s37, 0
	s_addc_u32 s13, s61, 0
	v_ashrrev_i32_e32 v144, 4, v0
	v_lshrrev_b32_e32 v0, 1, v86
	s_mov_b32 s6, 0x7ffffff0
	v_writelane_b32 v255, s76, 1
	s_add_u32 s0, s60, 0x22600000
	v_and_b32_e32 v124, 0x78, v0
	v_and_or_b32 v0, v121, s6, v84
	v_mov_b32_e32 v87, 0xffffff80
	v_writelane_b32 v255, s77, 2
	s_addc_u32 s1, s61, 0
	v_lshl_add_u32 v146, v0, 1, v87
	v_and_or_b32 v0, v132, s6, v84
	v_writelane_b32 v255, s0, 3
	v_lshl_add_u32 v147, v0, 1, v87
	v_and_or_b32 v0, v134, s6, v84
	v_writelane_b32 v255, s1, 4
	v_readlane_b32 s0, v254, 55
	v_lshl_add_u32 v148, v0, 1, v87
	v_and_or_b32 v0, v136, s6, v84
	s_lshl_b32 s0, s0, 4
	v_lshl_add_u32 v149, v0, 1, v87
	v_lshlrev_b32_e32 v0, 2, v2
	s_add_i32 s1, s0, 16
	s_add_i32 s2, s0, 32
	s_add_i32 s3, s0, 48
	s_add_i32 s4, s0, 64
	s_add_i32 s5, s0, 0x50
	s_add_i32 s8, s0, 0x60
	s_add_i32 s14, s0, 0x70
	s_add_i32 s15, s0, 0x80
	v_or_b32_e32 v123, s0, v84
	v_lshl_add_u32 v126, v2, 4, 0
	v_or_b32_e32 v150, s0, v0
	v_cmp_eq_u32_e64 s[46:47], 0, v2
	v_ashrrev_i32_e32 v2, 2, v86
	s_mov_b32 s0, 0x3ffffff0
	v_sub_u32_e32 v87, v0, v84
	v_and_or_b32 v151, v2, -16, v84
	v_lshrrev_b32_e32 v2, 1, v85
	v_and_or_b32 v85, v121, s0, v84
	s_movk_i32 s16, 0x81
	v_lshlrev_b32_e32 v152, 2, v85
	v_and_or_b32 v85, v132, s0, v84
	v_cmp_gt_u32_e64 s[6:7], s16, v87
	v_lshlrev_b32_e32 v153, 2, v85
	v_and_or_b32 v85, v134, s0, v84
	v_writelane_b32 v255, s6, 5
	v_lshlrev_b32_e32 v154, 2, v85
	v_and_or_b32 v85, v136, s0, v84
	v_writelane_b32 v255, s7, 6
	v_cmp_lt_i32_e64 s[6:7], s52, v150
	v_lshlrev_b32_e32 v155, 2, v85
	v_add_u32_e32 v85, 1, v87
	v_writelane_b32 v255, s6, 7
	s_movk_i32 s17, 0x7e
	v_or_b32_e32 v156, s1, v84
	v_writelane_b32 v255, s7, 8
	v_cmp_gt_u32_e64 s[6:7], s16, v85
	v_add_u32_e32 v85, 2, v87
	v_or_b32_e32 v158, s3, v84
	v_writelane_b32 v255, s6, 9
	v_or_b32_e32 v161, s8, v84
	v_or_b32_e32 v157, s2, v84
	v_writelane_b32 v255, s7, 10
	v_cmp_lt_i32_e64 s[6:7], s17, v150
	v_and_b32_e32 v2, 24, v2
	v_add_u32_e32 v127, 0xffffff80, v121
	v_writelane_b32 v255, s6, 11
	v_add_u32_e32 v133, 0xffffff80, v132
	v_add_u32_e32 v135, 0xffffff80, v134
	v_writelane_b32 v255, s7, 12
	v_cmp_gt_u32_e64 s[6:7], s16, v85
	v_or_b32_e32 v85, 2, v150
	v_add_u32_e32 v137, 0xffffff80, v136
	v_writelane_b32 v255, s6, 13
	v_add_u32_e32 v139, 0xffffff80, v138
	v_add_u32_e32 v141, 0xffffff80, v140
	v_writelane_b32 v255, s7, 14
	v_cmp_lt_i32_e64 s[6:7], s52, v85
	v_add_u32_e32 v85, 3, v87
	v_add_u32_e32 v143, 0xffffff80, v142
	v_writelane_b32 v255, s6, 15
	v_add_u32_e32 v145, 0xffffff80, v144
	s_mov_b32 s43, 0
	v_writelane_b32 v255, s7, 16
	v_cmp_gt_u32_e64 s[6:7], s16, v85
	v_or_b32_e32 v85, 3, v150
	v_or_b32_e32 v159, s4, v84
	v_writelane_b32 v255, s6, 17
	v_or_b32_e32 v160, s5, v84
	v_or_b32_e32 v163, s14, v84
	v_writelane_b32 v255, s7, 18
	v_cmp_lt_i32_e64 s[6:7], s52, v85
; #define LAS __attribute__((address_space(3)))
; __device__ __forceinline__ void ph_attn_mfma(const Frame& F) {
;     ...
;     const int tid = (F.wave * 64 + fresh_lane()), lane = tid & 63, wave = F.wave;
;     const int l15 = lane & 15, g = lane >> 4;
;     const float sc2 = 0.08838834764831845f * 1.4426950408889634f;
;     v4u kreg[8], va[4], vb[4], qn[4];
;     const int vb0 = (F.nwg % 8 == 0) ? ((F.bid % 8) * (F.nwg / 8) + F.bid / 8) : F.bid;
;     const int per = (3072 + F.nwg - 1) / F.nwg, ibase = vb0 * per, iend = (ibase + per < 3072) ? ibase + per : 3072;
;     int px = 0; AttnItem itp = attn_decode(0); bool havep = false;
;     if (ibase < iend) { const AttnItem it0 = attn_decode(ibase); attn_issue(HB, it0, tid, kreg, va, vb, false); attn_issue_q(HB, it0, tid, qn); }
;     for (int item = ibase; item < iend; ++item) {
;         const AttnItem it = attn_decode(item);
;         const bool cont = havep && attn_cont(it, itp);
;         px = cont ? (px ^ 1) : 0;
;         itp = it; havep = true;
;         const int hd = it.hd, br = it.br, dsh = it.dsh, blk = it.blk, tok0 = it.tok0;
;         const int qtok = tok0 + ((blk * 128 + wave * 16 + l15) << dsh);
;         v4u qf[4];
; #pragma unroll
;         for (int st = 0; st < 4; ++st) qf[st] = qn[st];
;         __syncthreads();
; #pragma unroll
;         for (int i = 0; i < 8; ++i) { if (cont && i < 4) continue; const int c = tid + 512 * i, kj = (c >> 4) ^ (px << 7), ch = c & 15; *(LAS v4u*)(lds + AT_K_OFF + kj * AT_KROW + ch * 16) = kreg[i]; }
; #pragma unroll
;         for (int i = 0; i < 4; ++i) {
;             if (cont && i < 2) continue;
;             const int u = tid + 512 * i;
;             const int kp = (((u >> 8) << 4) | (u & 15)) ^ (px << 6), ch = (((u >> 6) & 3) << 2) | ((u >> 4) & 3);
;             const v4u a = va[i], bb = vb[i];
;             LAS unsigned char* vbp = lds + AT_V_OFF + (ch * 8) * AT_VROW + kp * 4;
;             *(LAS unsigned*)(vbp + 0 * AT_VROW) = (a.x & 0xffffu) | (bb.x << 16);      *(LAS unsigned*)(vbp + 1 * AT_VROW) = (a.x >> 16) | (bb.x & 0xffff0000u);
;             *(LAS unsigned*)(vbp + 2 * AT_VROW) = (a.y & 0xffffu) | (bb.y << 16);      *(LAS unsigned*)(vbp + 3 * AT_VROW) = (a.y >> 16) | (bb.y & 0xffff0000u);
;             *(LAS unsigned*)(vbp + 4 * AT_VROW) = (a.z & 0xffffu) | (bb.z << 16);      *(LAS unsigned*)(vbp + 5 * AT_VROW) = (a.z >> 16) | (bb.z & 0xffff0000u);
	v_or_b32_e32 v85, s1, v0
	v_cmp_lt_i32_e64 s[0:1], s52, v85
	v_writelane_b32 v255, s6, 19
	v_or_b32_e32 v86, 2, v85
	v_or_b32_e32 v170, s15, v84
	v_writelane_b32 v255, s7, 20
	v_writelane_b32 v255, s0, 21
	v_add_u32_e32 v172, 16, v150
	v_add_u32_e32 v173, 32, v150
	v_writelane_b32 v255, s1, 22
	v_cmp_lt_i32_e64 s[0:1], s17, v85
	v_or_b32_e32 v85, 3, v85
	v_add_u32_e32 v174, 48, v150
	v_writelane_b32 v255, s0, 23
	v_add_u32_e32 v175, 64, v150
	v_add_u32_e32 v176, 0x50, v150
	v_writelane_b32 v255, s1, 24
	v_cmp_lt_i32_e64 s[0:1], s52, v86
	v_add_u32_e32 v177, 0x60, v150
	v_add_u32_e32 v178, 0x70, v150
	v_writelane_b32 v255, s0, 25
	v_add_u32_e32 v179, 0x80, v150
	s_lshl_b32 s36, s39, 7
	v_writelane_b32 v255, s1, 26
	v_cmp_lt_i32_e64 s[0:1], s52, v85
	v_or_b32_e32 v85, s2, v0
	v_or_b32_e32 v86, 2, v85
	v_writelane_b32 v255, s0, 27
	s_movk_i32 s2, 0xff7e
	v_cmp_lt_u32_e64 s[80:81], s2, v87
	v_writelane_b32 v255, s1, 28
	v_cmp_lt_i32_e64 s[0:1], s52, v85
	s_movk_i32 s2, 0x210
	v_mad_u32_u24 v171, v84, s2, v3
	v_writelane_b32 v255, s0, 29
	s_mov_b64 s[20:21], 0
	v_lshlrev_b32_e32 v128, 1, v0
	v_writelane_b32 v255, s1, 30
	v_cmp_lt_i32_e64 s[0:1], s17, v85
	v_or_b32_e32 v85, 3, v85
	v_lshlrev_b32_e32 v130, 1, v2
	v_writelane_b32 v255, s0, 31
	s_mov_b32 s2, 0
	s_nop 0
	v_writelane_b32 v255, s1, 32
	v_cmp_lt_i32_e64 s[0:1], s52, v86
	s_nop 1
	v_writelane_b32 v255, s0, 33
	s_nop 1
	v_writelane_b32 v255, s1, 34
	v_cmp_lt_i32_e64 s[0:1], s52, v85
	v_or_b32_e32 v85, s3, v0
	v_or_b32_e32 v86, 2, v85
	v_writelane_b32 v255, s0, 35
	s_movk_i32 s3, 0x7f
	s_nop 0
	v_writelane_b32 v255, s1, 36
	v_cmp_lt_i32_e64 s[0:1], s52, v85
	s_nop 1
	v_writelane_b32 v255, s0, 37
	s_nop 1
	v_writelane_b32 v255, s1, 38
	v_cmp_lt_i32_e64 s[0:1], s17, v85
	v_or_b32_e32 v85, 3, v85
	s_nop 0
	v_writelane_b32 v255, s0, 39
	s_nop 1
	v_writelane_b32 v255, s1, 40
	v_cmp_lt_i32_e64 s[0:1], s52, v86
	s_nop 1
	v_writelane_b32 v255, s0, 41
	s_nop 1
	v_writelane_b32 v255, s1, 42
	v_cmp_lt_i32_e64 s[0:1], s52, v85
	v_or_b32_e32 v85, s4, v0
	v_or_b32_e32 v86, 2, v85
	v_writelane_b32 v255, s0, 43
	v_cmp_lt_i32_e64 s[48:49], s52, v86
	s_mov_b32 s4, 0
	v_writelane_b32 v255, s1, 44
	v_cmp_lt_i32_e64 s[0:1], s52, v85
	s_nop 1
	v_writelane_b32 v255, s0, 45
	s_nop 1
	v_writelane_b32 v255, s1, 46
	v_cmp_lt_i32_e64 s[0:1], s17, v85
	v_or_b32_e32 v85, 3, v85
	v_cmp_lt_i32_e64 s[50:51], s52, v85
	v_or_b32_e32 v85, s5, v0
	v_cmp_lt_i32_e64 s[52:53], s52, v85
	v_cmp_lt_i32_e64 s[54:55], s17, v85
	v_or_b32_e32 v86, 2, v85
	v_or_b32_e32 v85, 3, v85
	v_cmp_lt_i32_e64 s[6:7], s3, v85
	v_or_b32_e32 v85, s8, v0
	v_cmp_lt_i32_e64 s[56:57], s3, v86
	v_cmp_lt_i32_e64 s[8:9], s3, v85
	v_cmp_lt_i32_e64 s[62:63], s17, v85
	v_or_b32_e32 v86, 2, v85
	v_or_b32_e32 v85, 3, v85
	v_writelane_b32 v255, s0, 47
	v_cmp_lt_i32_e64 s[28:29], s3, v85
	v_or_b32_e32 v85, s14, v0
	v_writelane_b32 v255, s1, 48
	v_cmp_lt_i32_e64 s[26:27], s3, v86
	v_cmp_lt_i32_e64 s[0:1], s3, v85
	v_cmp_lt_i32_e64 s[70:71], s17, v85
	v_or_b32_e32 v86, 2, v85
	v_or_b32_e32 v85, 3, v85
	v_cmp_lt_i32_e64 s[74:75], s3, v85
	v_add_u32_e32 v85, 0x80, v87
	v_cmp_lt_i32_e64 s[72:73], s3, v86
	v_or_b32_e32 v86, s15, v0
	v_cmp_gt_u32_e64 s[76:77], s16, v85
	v_add_u32_e32 v85, 0x82, v87
	v_cmp_gt_u32_e64 s[84:85], s16, v85
	v_or_b32_e32 v85, 2, v86
	v_cmp_lt_i32_e64 s[86:87], s3, v85
	v_add_u32_e32 v85, 0x83, v87
	v_cmp_gt_u32_e64 s[88:89], s16, v85
	v_or_b32_e32 v85, 3, v86
	v_cmp_lt_i32_e64 s[78:79], s3, v86
	v_cmp_lt_i32_e64 s[82:83], s17, v86
	v_cmp_lt_i32_e64 s[90:91], s3, v85
	s_mov_b32 s3, 0
	s_mov_b32 s5, 0
	s_waitcnt vmcnt(0)
	s_branch .LBB0_861

; #define LAS __attribute__((address_space(3)))
; __device__ __forceinline__ void ph_attn_mfma(const Frame& F) {
;     ...
;     for (int item = ibase; item < iend; ++item) {
;         const AttnItem it = attn_decode(item);
;         const bool cont = havep && attn_cont(it, itp);
;         px = cont ? (px ^ 1) : 0;
;         itp = it; havep = true;
;         const int hd = it.hd, br = it.br, dsh = it.dsh, blk = it.blk, tok0 = it.tok0;
;         const int qtok = tok0 + ((blk * 128 + wave * 16 + l15) << dsh);
;         v4u qf[4];
; #pragma unroll
;         for (int st = 0; st < 4; ++st) qf[st] = qn[st];
;         __syncthreads();
; #pragma unroll
;         for (int i = 0; i < 8; ++i) { if (cont && i < 4) continue; const int c = tid + 512 * i, kj = (c >> 4) ^ (px << 7), ch = c & 15; *(LAS v4u*)(lds + AT_K_OFF + kj * AT_KROW + ch * 16) = kreg[i]; }
.LBB0_863:
	s_xor_b32 s2, s43, 1
	s_and_b64 vcc, s[18:19], exec
	s_cselect_b32 s43, s2, 0
	s_lshl_b32 s15, s43, 7
	s_waitcnt vmcnt(8) lgkmcnt(0)
	v_mov_b32_e32 v52, v212
	v_mov_b32_e32 v53, v213
	v_mov_b32_e32 v54, v214
	v_mov_b32_e32 v55, v215
	v_mov_b32_e32 v56, v216
	v_mov_b32_e32 v57, v217
	v_mov_b32_e32 v58, v218
	v_mov_b32_e32 v59, v219
	v_mov_b32_e32 v60, v220
	v_mov_b32_e32 v61, v221
	v_mov_b32_e32 v62, v222
	v_mov_b32_e32 v63, v223
	v_mov_b32_e32 v64, v224
	v_mov_b32_e32 v65, v225
	v_mov_b32_e32 v66, v226
	v_mov_b32_e32 v67, v227
	s_barrier
	s_cbranch_vccnz .LBB0_865
	v_xor_b32_e32 v0, s15, v121
	s_movk_i32 s4, 0x110
	v_mad_u64_u32 v[2:3], s[2:3], v0, s4, v[122:123]
	v_xor_b32_e32 v0, s15, v132
	ds_write_b128 v2, v[8:11]
	v_mad_u64_u32 v[2:3], s[2:3], v0, s4, v[122:123]
	v_xor_b32_e32 v0, s15, v134
	ds_write_b128 v2, v[4:7]
	v_mad_u64_u32 v[2:3], s[2:3], v0, s4, v[122:123]
	v_xor_b32_e32 v0, s15, v136
	ds_write_b128 v2, v[12:15]
	v_mad_u64_u32 v[2:3], s[2:3], v0, s4, v[122:123]
	ds_write_b128 v2, v[16:19]
